# MoE unit scheduler: expert-of-tile table staged in LDS once per phase and tile count kept in an SGPR, replacing two dependent global loads + vmcnt(0) per unit; gidx prefetch; hand-written weight conve
# speedup vs baseline: 1.0164x; 1.0164x over previous
.LBB0_2254:
	s_cmp_lt_i32 s92, 13
	s_cselect_b64 s[0:1], -1, 0
	s_cmp_gt_i32 s93, 12
	s_cselect_b64 s[2:3], -1, 0
	s_and_b64 s[0:1], s[0:1], s[2:3]
	v_cndmask_b32_e64 v0, 0, 1, s[0:1]
	v_cmp_ne_u32_e64 s[4:5], 1, v0
	s_andn2_b64 vcc, exec, s[0:1]
	v_mbcnt_lo_u32_b32 v0, -1, 0
	v_mbcnt_hi_u32_b32 v0, -1, v0
	s_cbranch_vccnz .LBB0_2288
	v_mbcnt_lo_u32_b32 v0, -1, 0
	v_mbcnt_hi_u32_b32 v0, -1, v0
	v_add_u32_e32 v0, s52, v0
	v_lshlrev_b32_e32 v0, 2, v0
	s_add_u32 s6, s26, 0xf00000
	s_addc_u32 s7, s27, 0
	global_load_dword v1, v0, s[6:7]
	global_load_dword v2, v0, s[6:7] offset:2048
	v_add_u32_e32 v0, 0x20000, v0
	s_waitcnt vmcnt(0)
	ds_write_b32 v0, v1
	ds_write_b32 v0, v2 offset:2048
	s_waitcnt lgkmcnt(0)
	s_barrier
	s_mov_b32 s0, 16
	s_waitcnt lgkmcnt(0)
	v_mov_b32_e32 v1, 0xf01000
	v_mbcnt_lo_u32_b32 v0, -1, 0
	v_mbcnt_hi_u32_b32 v0, -1, v0
	global_load_dword v2, v1, s[26:27]
	s_ashr_i32 s95, s94, 31
	s_add_u32 s8, s26, 0xf01000
	v_add_u32_e32 v1, s52, v0
	s_addc_u32 s9, s27, 0
	v_readfirstlane_b32 s16, v1
	s_waitcnt vmcnt(0)
	v_ashrrev_i32_e32 v3, 31, v2
	v_readfirstlane_b32 s2, v2
	s_mov_b32 s98, s2
	v_lshlrev_b64 v[2:3], 4, v[2:3]
	v_cmp_ge_i64_e32 vcc, s[94:95], v[2:3]
	s_cbranch_vccnz .LBB0_2288
	s_lshr_b32 s1, s95, 29
	s_add_i32 s1, s94, s1
	s_ashr_i32 s3, s1, 3
	s_and_b32 s1, s1, -8
	s_sub_i32 s1, s94, s1
	v_mov_b32_e32 v2, s1
	v_alignbit_b32 v2, s2, v2, 31
	s_nop 0
	v_readfirstlane_b32 s6, v2
	s_mul_i32 s1, s6, s1
	s_add_i32 s6, s1, s3
	s_ashr_i32 s1, s6, 31
	s_lshr_b32 s1, s1, 25
	s_add_i32 s7, s6, s1
	s_ashr_i32 s1, s7, 7
	s_lshl_b32 s1, s1, 3
	s_sub_i32 s3, s2, s1
	s_and_b32 s2, s7, 0xffffff80
	s_sub_i32 s2, s6, s2
	s_cmp_lt_i32 s3, 8
	s_cbranch_scc0 .LBB0_2258
	s_abs_i32 s6, s3
	v_cvt_f32_u32_e32 v2, s6
	s_sub_i32 s11, 0, s6
	s_abs_i32 s10, s2
	s_xor_b32 s7, s2, s3
	v_rcp_iflag_f32_e32 v2, v2
	s_ashr_i32 s7, s7, 31
	v_mul_f32_e32 v2, 0x4f7ffffe, v2
	v_cvt_u32_f32_e32 v2, v2
	s_nop 0
	v_readfirstlane_b32 s12, v2
	s_mul_i32 s11, s11, s12
	s_mul_hi_u32 s11, s12, s11
	s_add_i32 s12, s12, s11
	s_mul_hi_u32 s11, s10, s12
	s_mul_i32 s12, s11, s6
	s_sub_i32 s10, s10, s12
	s_add_i32 s13, s11, 1
	s_sub_i32 s12, s10, s6
	s_cmp_ge_u32 s10, s6
	s_cselect_b32 s11, s13, s11
	s_cselect_b32 s10, s12, s10
	s_add_i32 s12, s11, 1
	s_cmp_ge_u32 s10, s6
	s_cselect_b32 s6, s12, s11
	s_xor_b32 s6, s6, s7
	s_sub_i32 s6, s6, s7
	s_mul_i32 s3, s6, s3
	s_sub_i32 s3, s2, s3
	s_add_i32 s14, s3, s1
	s_cbranch_execz .LBB0_2259
	s_branch .LBB0_2260

.LBB0_2265:
	s_mov_b32 s6, s71
	s_add_i32 s71, s71, 1
	s_cmp_gt_u32 s6, 0x3ffffffe
	s_cbranch_scc1 .LBB0_2272
	v_mov_b32_e32 v0, s98
	s_load_dword s30, s[90:91], 0x100
	s_mul_i32 s6, s71, s72
	s_waitcnt lgkmcnt(0)
	s_mul_hi_u32 s7, s71, s30
	s_mul_i32 s30, s71, s30
	s_add_i32 s7, s7, s6
	s_add_u32 s6, s30, s94
	s_addc_u32 s7, s7, s95
	v_ashrrev_i32_e32 v1, 31, v0
	v_readfirstlane_b32 s30, v0
	v_lshlrev_b64 v[0:1], 4, v[0:1]
	v_cmp_ge_i64_e32 vcc, s[6:7], v[0:1]
	s_cbranch_vccnz .LBB0_2273
	s_ashr_i32 s7, s6, 31
	s_lshr_b32 s7, s7, 29
	s_add_i32 s7, s6, s7
	s_ashr_i32 s22, s7, 3
	s_and_b32 s7, s7, -8
	s_sub_i32 s6, s6, s7
	v_mov_b32_e32 v0, s6
	v_alignbit_b32 v0, s30, v0, 31
	s_nop 0
	v_readfirstlane_b32 s7, v0
	s_mul_i32 s6, s7, s6
	s_add_i32 s6, s6, s22
	s_ashr_i32 s7, s6, 31
	s_lshr_b32 s7, s7, 25
	s_add_i32 s22, s6, s7
	s_ashr_i32 s7, s22, 7
	s_lshl_b32 s7, s7, 3
	s_and_b32 s22, s22, 0xffffff80
	s_sub_i32 s29, s30, s7
	s_sub_i32 s28, s6, s22
	s_cmp_lt_i32 s29, 8
	s_mov_b64 s[22:23], -1
	s_cbranch_scc0 .LBB0_2269
	s_abs_i32 s6, s29
	v_cvt_f32_u32_e32 v0, s6
	s_sub_i32 s30, 0, s6
	s_abs_i32 s23, s28
	s_xor_b32 s22, s28, s29
	v_rcp_iflag_f32_e32 v0, v0
	s_ashr_i32 s22, s22, 31
	v_mul_f32_e32 v0, 0x4f7ffffe, v0
	v_cvt_u32_f32_e32 v0, v0
	s_nop 0
	v_readfirstlane_b32 s31, v0
	s_mul_i32 s30, s30, s31
	s_mul_hi_u32 s30, s31, s30
	s_add_i32 s31, s31, s30
	s_mul_hi_u32 s30, s23, s31
	s_mul_i32 s31, s30, s6
	s_sub_i32 s23, s23, s31
	s_add_i32 s34, s30, 1
	s_sub_i32 s31, s23, s6
	s_cmp_ge_u32 s23, s6
	s_cselect_b32 s30, s34, s30
	s_cselect_b32 s23, s31, s23
	s_add_i32 s31, s30, 1
	s_cmp_ge_u32 s23, s6
	s_cselect_b32 s6, s31, s30
	s_xor_b32 s6, s6, s22
	s_sub_i32 s6, s6, s22
	s_mul_i32 s22, s6, s29
	s_sub_i32 s22, s28, s22
	s_add_i32 s34, s22, s7
	s_mov_b64 s[22:23], 0

.LBB0_2271:
	s_ashr_i32 s35, s34, 31
	s_lshl_b64 s[22:23], s[34:35], 2
	s_add_i32 s22, s22, 0x20000
	v_mov_b32_e32 v186, s22
	ds_read_b32 v186, v186
	s_lshl_b32 s22, s34, 8
	s_ashr_i32 s23, s22, 31
	s_lshl_b64 s[22:23], s[22:23], 2
	s_mov_b64 s[48:49], -1
	s_waitcnt lgkmcnt(0)
	v_readfirstlane_b32 s28, v186
	s_ashr_i32 s29, s28, 31
	s_add_u32 s30, s3, s22
	s_addc_u32 s31, s19, s23
	s_ashr_i32 s7, s6, 31
	s_lshl_b64 s[28:29], s[28:29], 22
	s_lshl_b64 s[36:37], s[6:7], 18
	s_add_u32 s22, s21, s36
	s_addc_u32 s23, s33, s37
	s_add_u32 s22, s22, s28
	s_addc_u32 s23, s23, s29
	s_add_u32 s28, s58, s28
	s_addc_u32 s29, s59, s29
	s_add_u32 s28, s28, s36
	s_addc_u32 s29, s29, s37
	s_lshl_b64 s[34:35], s[34:35], 19
	s_lshl_b64 s[36:37], s[6:7], 7
	s_add_u32 s7, s69, s34
	s_addc_u32 s35, s70, s35
	s_add_u32 s34, s7, s36
	s_addc_u32 s35, s35, s37
	s_lshl_b32 s78, s6, 7
	s_branch .LBB0_2274

.LBB0_2276:
	s_andn2_b64 vcc, exec, s[14:15]
	s_cbranch_vccnz .LBB0_2281
	s_add_u32 s47, s50, 0x100
	s_addc_u32 s79, s51, 0
	s_add_u32 s80, s52, 0x100
	s_addc_u32 s81, s53, 0
	s_add_u32 s56, s56, 0x100
	s_addc_u32 s57, s57, 0
	s_add_u32 s82, s54, 0x100
	v_mov_b32_e32 v32, 0
	v_lshl_add_u64 v[166:167], v[160:161], 2, s[30:31]
	v_lshl_add_u64 v[168:169], v[162:163], 2, s[30:31]
	s_addc_u32 s83, s55, 0
	s_mov_b32 s84, 0
	s_cmp_eq_u64 s[48:49], 0
	s_cbranch_scc1 .Lgx_skip
	global_load_dword v252, v[166:167], off
	global_load_dword v253, v[168:169], off
	global_load_dword v168, v[168:169], off offset:512
	global_load_dword v166, v[166:167], off offset:512
.Lgx_skip:
	v_mov_b32_e32 v33, v32
	v_mov_b32_e32 v34, v32
	v_mov_b32_e32 v35, v32
	v_mov_b32_e32 v56, v32
	v_mov_b32_e32 v57, v32
	v_mov_b32_e32 v58, v32
	v_mov_b32_e32 v59, v32
	v_mov_b32_e32 v48, v32
	v_mov_b32_e32 v49, v32
	v_mov_b32_e32 v50, v32
	v_mov_b32_e32 v51, v32
	v_mov_b32_e32 v40, v32
	v_mov_b32_e32 v41, v32
	v_mov_b32_e32 v42, v32
	v_mov_b32_e32 v43, v32
	v_mov_b32_e32 v64, v32
	v_mov_b32_e32 v65, v32
	v_mov_b32_e32 v66, v32
	v_mov_b32_e32 v67, v32
	v_mov_b32_e32 v72, v32
	v_mov_b32_e32 v73, v32
	v_mov_b32_e32 v74, v32
	v_mov_b32_e32 v75, v32
	v_mov_b32_e32 v80, v32
	v_mov_b32_e32 v81, v32
	v_mov_b32_e32 v82, v32
	v_mov_b32_e32 v83, v32
	v_mov_b32_e32 v88, v32
	v_mov_b32_e32 v89, v32
	v_mov_b32_e32 v90, v32
	v_mov_b32_e32 v91, v32
	v_mov_b32_e32 v36, v32
	v_mov_b32_e32 v37, v32
	v_mov_b32_e32 v38, v32
	v_mov_b32_e32 v39, v32
	v_mov_b32_e32 v60, v32
	v_mov_b32_e32 v61, v32
	v_mov_b32_e32 v62, v32
	v_mov_b32_e32 v63, v32
	v_mov_b32_e32 v52, v32
	v_mov_b32_e32 v53, v32
	v_mov_b32_e32 v54, v32
	v_mov_b32_e32 v55, v32
	v_mov_b32_e32 v44, v32
	v_mov_b32_e32 v45, v32
	v_mov_b32_e32 v46, v32
	v_mov_b32_e32 v47, v32
	v_mov_b32_e32 v68, v32
	v_mov_b32_e32 v69, v32
	v_mov_b32_e32 v70, v32
	v_mov_b32_e32 v71, v32
	v_mov_b32_e32 v76, v32
	v_mov_b32_e32 v77, v32
	v_mov_b32_e32 v78, v32
	v_mov_b32_e32 v79, v32
	v_mov_b32_e32 v84, v32
	v_mov_b32_e32 v85, v32
	v_mov_b32_e32 v86, v32
	v_mov_b32_e32 v87, v32
	v_mov_b32_e32 v92, v32
	v_mov_b32_e32 v93, v32
	v_mov_b32_e32 v94, v32
	v_mov_b32_e32 v95, v32
	v_mov_b32_e32 v96, v32
	v_mov_b32_e32 v97, v32
	v_mov_b32_e32 v98, v32
	v_mov_b32_e32 v99, v32
	v_mov_b32_e32 v104, v32
	v_mov_b32_e32 v105, v32
	v_mov_b32_e32 v106, v32
	v_mov_b32_e32 v107, v32
	v_mov_b32_e32 v112, v32
	v_mov_b32_e32 v113, v32
	v_mov_b32_e32 v114, v32
	v_mov_b32_e32 v115, v32
	v_mov_b32_e32 v120, v32
	v_mov_b32_e32 v121, v32
	v_mov_b32_e32 v122, v32
	v_mov_b32_e32 v123, v32
	v_mov_b32_e32 v128, v32
	v_mov_b32_e32 v129, v32
	v_mov_b32_e32 v130, v32
	v_mov_b32_e32 v131, v32
	v_mov_b32_e32 v136, v32
	v_mov_b32_e32 v137, v32
	v_mov_b32_e32 v138, v32
	v_mov_b32_e32 v139, v32
	v_mov_b32_e32 v144, v32
	v_mov_b32_e32 v145, v32
	v_mov_b32_e32 v146, v32
	v_mov_b32_e32 v147, v32
	v_mov_b32_e32 v152, v32
	v_mov_b32_e32 v153, v32
	v_mov_b32_e32 v154, v32
	v_mov_b32_e32 v155, v32
	v_mov_b32_e32 v100, v32
	v_mov_b32_e32 v101, v32
	v_mov_b32_e32 v102, v32
	v_mov_b32_e32 v103, v32
	v_mov_b32_e32 v108, v32
	v_mov_b32_e32 v109, v32
	v_mov_b32_e32 v110, v32
	v_mov_b32_e32 v111, v32
	v_mov_b32_e32 v116, v32
	v_mov_b32_e32 v117, v32
	v_mov_b32_e32 v118, v32
	v_mov_b32_e32 v119, v32
	v_mov_b32_e32 v124, v32
	v_mov_b32_e32 v125, v32
	v_mov_b32_e32 v126, v32
	v_mov_b32_e32 v127, v32
	v_mov_b32_e32 v132, v32
	v_mov_b32_e32 v133, v32
	v_mov_b32_e32 v134, v32
	v_mov_b32_e32 v135, v32
	v_mov_b32_e32 v140, v32
	v_mov_b32_e32 v141, v32
	v_mov_b32_e32 v142, v32
	v_mov_b32_e32 v143, v32
	v_mov_b32_e32 v148, v32
	v_mov_b32_e32 v149, v32
	v_mov_b32_e32 v150, v32
	v_mov_b32_e32 v151, v32
	v_mov_b32_e32 v156, v32
	v_mov_b32_e32 v157, v32
	v_mov_b32_e32 v158, v32
	v_mov_b32_e32 v159, v32
	s_branch .LBB0_2279

.LBB0_2279:
	ds_read_b128 v[16:19], v182
	ds_read_b128 v[20:23], v182 offset:1024
	ds_read_b128 v[24:27], v182 offset:2048
	ds_read_b128 v[28:31], v182 offset:3072
	ds_read_b128 v[0:3], v183
	ds_read_b128 v[4:7], v183 offset:1024
	ds_read_b128 v[8:11], v183 offset:2048
	ds_read_b128 v[12:15], v183 offset:3072
	s_cmp_eq_u32 s75, s84
	s_cselect_b64 s[50:51], -1, 0
	s_add_u32 s52, s82, 0xffffff80
	s_addc_u32 s53, s83, -1
	v_mov_b32_e32 v165, v177
	v_mov_b32_e32 v187, v178
	s_add_i32 m0, s61, 0xc000
	ds_read_b128 v[188:191], v184
	ds_read_b128 v[192:195], v184 offset:1024
	ds_read_b128 v[196:199], v184 offset:2048
	ds_read_b128 v[200:203], v184 offset:3072
	ds_read_b128 v[204:207], v184 offset:4096
	ds_read_b128 v[208:211], v184 offset:5120
	ds_read_b128 v[212:215], v184 offset:6144
	ds_read_b128 v[216:219], v184 offset:7168
	s_nop 0
	global_load_lds_dwordx4 v165, s[52:53]
	s_add_i32 m0, s61, 0xe000
	s_nop 0
	global_load_lds_dwordx4 v187, s[52:53]
	s_waitcnt vmcnt(8)
	s_waitcnt lgkmcnt(0)
	s_barrier
	s_setprio 0
	s_waitcnt lgkmcnt(0)
	v_mfma_f32_16x16x128_f8f6f4 v[156:159], v[16:23], v[188:195], v[156:159]
	v_mfma_f32_16x16x128_f8f6f4 v[148:151], v[24:31], v[188:195], v[148:151]
	v_mfma_f32_16x16x128_f8f6f4 v[140:143], v[16:23], v[196:203], v[140:143]
	v_mfma_f32_16x16x128_f8f6f4 v[132:135], v[24:31], v[196:203], v[132:135]
	v_mfma_f32_16x16x128_f8f6f4 v[124:127], v[16:23], v[204:211], v[124:127]
	v_mfma_f32_16x16x128_f8f6f4 v[116:119], v[24:31], v[204:211], v[116:119]
	v_mfma_f32_16x16x128_f8f6f4 v[108:111], v[16:23], v[212:219], v[108:111]
	v_mfma_f32_16x16x128_f8f6f4 v[100:103], v[24:31], v[212:219], v[100:103]
	s_setprio 1
	s_setprio 0
	v_mfma_f32_16x16x128_f8f6f4 v[152:155], v[0:7], v[188:195], v[152:155]
	v_mfma_f32_16x16x128_f8f6f4 v[144:147], v[8:15], v[188:195], v[144:147]
	v_mfma_f32_16x16x128_f8f6f4 v[136:139], v[0:7], v[196:203], v[136:139]
	v_mfma_f32_16x16x128_f8f6f4 v[128:131], v[8:15], v[196:203], v[128:131]
	v_mfma_f32_16x16x128_f8f6f4 v[120:123], v[0:7], v[204:211], v[120:123]
	v_mfma_f32_16x16x128_f8f6f4 v[112:115], v[8:15], v[204:211], v[112:115]
	v_mfma_f32_16x16x128_f8f6f4 v[104:107], v[0:7], v[212:219], v[104:107]
	v_mfma_f32_16x16x128_f8f6f4 v[96:99], v[8:15], v[212:219], v[96:99]
	s_setprio 1
	s_barrier
	s_and_b64 s[52:53], s[48:49], s[50:51]
	s_andn2_b64 vcc, exec, s[52:53]
	s_cbranch_vccnz .LBB0_2278
	v_lshl_add_u32 v175, v252, 11, v171
	v_lshl_add_u32 v176, v253, 11, v173
	v_lshl_add_u32 v178, v168, 11, v173
	v_lshl_add_u32 v177, v166, 11, v171
	s_branch .LBB0_2278

.LBB0_2341:
	s_cmp_lt_i32 s92, 14
	s_cselect_b64 s[0:1], -1, 0
	s_cmp_gt_i32 s93, 13
	s_cselect_b64 s[2:3], -1, 0
	s_and_b64 s[0:1], s[0:1], s[2:3]
	v_cndmask_b32_e64 v0, 0, 1, s[0:1]
	v_cmp_ne_u32_e64 s[4:5], 1, v0
	s_andn2_b64 vcc, exec, s[0:1]
	v_mbcnt_lo_u32_b32 v0, -1, 0
	v_mbcnt_hi_u32_b32 v0, -1, v0
	s_cbranch_vccnz .LBB0_2373
	v_mbcnt_lo_u32_b32 v0, -1, 0
	v_mbcnt_hi_u32_b32 v0, -1, v0
	v_add_u32_e32 v0, s52, v0
	v_lshlrev_b32_e32 v0, 2, v0
	s_add_u32 s6, s26, 0xf00000
	s_addc_u32 s7, s27, 0
	global_load_dword v1, v0, s[6:7]
	global_load_dword v2, v0, s[6:7] offset:2048
	v_add_u32_e32 v0, 0x20000, v0
	s_waitcnt vmcnt(0)
	ds_write_b32 v0, v1
	ds_write_b32 v0, v2 offset:2048
	s_waitcnt lgkmcnt(0)
	s_barrier
	s_mov_b32 s0, 16
	s_waitcnt lgkmcnt(0)
	v_mov_b32_e32 v1, 0xf01000
	v_mbcnt_lo_u32_b32 v0, -1, 0
	v_mbcnt_hi_u32_b32 v0, -1, v0
	global_load_dword v2, v1, s[26:27]
	s_ashr_i32 s95, s94, 31
	s_add_u32 s8, s26, 0xf01000
	v_add_u32_e32 v1, s52, v0
	s_addc_u32 s9, s27, 0
	v_readfirstlane_b32 s16, v1
	s_waitcnt vmcnt(0)
	v_ashrrev_i32_e32 v3, 31, v2
	v_readfirstlane_b32 s2, v2
	s_mov_b32 s98, s2
	v_lshlrev_b64 v[2:3], 3, v[2:3]
	v_cmp_ge_i64_e32 vcc, s[94:95], v[2:3]
	s_cbranch_vccnz .LBB0_2373
	s_lshr_b32 s1, s95, 29
	s_add_i32 s1, s94, s1
	s_ashr_i32 s3, s1, 3
	s_and_b32 s1, s1, -8
	s_sub_i32 s1, s94, s1
	s_lshr_b32 s6, s1, 31
	s_add_i32 s6, s2, s6
	s_mul_i32 s1, s6, s1
	s_add_i32 s6, s1, s3
	s_ashr_i32 s1, s6, 31
	s_lshr_b32 s1, s1, 26
	s_add_i32 s7, s6, s1
	s_ashr_i32 s1, s7, 6
	s_lshl_b32 s1, s1, 3
	s_andn2_b32 s7, s7, 63
	s_sub_i32 s3, s2, s1
	s_sub_i32 s2, s6, s7
	s_cmp_lt_i32 s3, 8
	s_cbranch_scc0 .LBB0_2345
	s_abs_i32 s6, s3
	v_cvt_f32_u32_e32 v2, s6
	s_sub_i32 s11, 0, s6
	s_abs_i32 s10, s2
	s_xor_b32 s7, s2, s3
	v_rcp_iflag_f32_e32 v2, v2
	s_ashr_i32 s7, s7, 31
	v_mul_f32_e32 v2, 0x4f7ffffe, v2
	v_cvt_u32_f32_e32 v2, v2
	s_nop 0
	v_readfirstlane_b32 s12, v2
	s_mul_i32 s11, s11, s12
	s_mul_hi_u32 s11, s12, s11
	s_add_i32 s12, s12, s11
	s_mul_hi_u32 s11, s10, s12
	s_mul_i32 s12, s11, s6
	s_sub_i32 s10, s10, s12
	s_add_i32 s13, s11, 1
	s_sub_i32 s12, s10, s6
	s_cmp_ge_u32 s10, s6
	s_cselect_b32 s11, s13, s11
	s_cselect_b32 s10, s12, s10
	s_add_i32 s12, s11, 1
	s_cmp_ge_u32 s10, s6
	s_cselect_b32 s6, s12, s11
	s_xor_b32 s6, s6, s7
	s_sub_i32 s6, s6, s7
	s_mul_i32 s3, s6, s3
	s_sub_i32 s3, s2, s3
	s_add_i32 s12, s3, s1
	s_cbranch_execz .LBB0_2346
	s_branch .LBB0_2347

.LBB0_2352:
	s_mov_b32 s6, s62
	s_add_i32 s62, s62, 1
	s_cmp_gt_u32 s6, 0x3ffffffe
	s_cbranch_scc1 .LBB0_2359
	v_mov_b32_e32 v0, s98
	s_load_dword s34, s[90:91], 0x100
	s_mul_i32 s6, s62, s68
	s_waitcnt lgkmcnt(0)
	s_mul_hi_u32 s7, s62, s34
	s_mul_i32 s34, s62, s34
	s_add_i32 s7, s7, s6
	s_add_u32 s6, s34, s94
	s_addc_u32 s7, s7, s95
	v_ashrrev_i32_e32 v1, 31, v0
	v_readfirstlane_b32 s34, v0
	v_lshlrev_b64 v[0:1], 3, v[0:1]
	v_cmp_ge_i64_e32 vcc, s[6:7], v[0:1]
	s_cbranch_vccnz .LBB0_2360
	s_ashr_i32 s7, s6, 31
	s_lshr_b32 s7, s7, 29
	s_add_i32 s7, s6, s7
	s_ashr_i32 s20, s7, 3
	s_and_b32 s7, s7, -8
	s_sub_i32 s6, s6, s7
	s_lshr_b32 s7, s6, 31
	s_add_i32 s7, s34, s7
	s_mul_i32 s6, s7, s6
	s_add_i32 s6, s6, s20
	s_ashr_i32 s7, s6, 31
	s_lshr_b32 s7, s7, 26
	s_add_i32 s20, s6, s7
	s_ashr_i32 s7, s20, 6
	s_lshl_b32 s7, s7, 3
	s_andn2_b32 s20, s20, 63
	s_sub_i32 s23, s34, s7
	s_sub_i32 s22, s6, s20
	s_cmp_lt_i32 s23, 8
	s_mov_b64 s[20:21], -1
	s_cbranch_scc0 .LBB0_2356
	s_abs_i32 s6, s23
	v_cvt_f32_u32_e32 v0, s6
	s_sub_i32 s28, 0, s6
	s_abs_i32 s21, s22
	s_xor_b32 s20, s22, s23
	v_rcp_iflag_f32_e32 v0, v0
	s_ashr_i32 s20, s20, 31
	v_mul_f32_e32 v0, 0x4f7ffffe, v0
	v_cvt_u32_f32_e32 v0, v0
	s_nop 0
	v_readfirstlane_b32 s29, v0
	s_mul_i32 s28, s28, s29
	s_mul_hi_u32 s28, s29, s28
	s_add_i32 s29, s29, s28
	s_mul_hi_u32 s28, s21, s29
	s_mul_i32 s29, s28, s6
	s_sub_i32 s21, s21, s29
	s_add_i32 s30, s28, 1
	s_sub_i32 s29, s21, s6
	s_cmp_ge_u32 s21, s6
	s_cselect_b32 s28, s30, s28
	s_cselect_b32 s21, s29, s21
	s_add_i32 s29, s28, 1
	s_cmp_ge_u32 s21, s6
	s_cselect_b32 s6, s29, s28
	s_xor_b32 s6, s6, s20
	s_sub_i32 s6, s6, s20
	s_mul_i32 s20, s6, s23
	s_sub_i32 s20, s22, s20
	s_add_i32 s34, s20, s7
	s_mov_b64 s[20:21], 0

.LBB0_2358:
	s_ashr_i32 s35, s34, 31
	s_lshl_b64 s[20:21], s[34:35], 2
	s_add_i32 s20, s20, 0x20000
	v_mov_b32_e32 v189, s20
	ds_read_b32 v189, v189
	s_lshl_b64 s[30:31], s[34:35], 19
	s_waitcnt lgkmcnt(0)
	v_readfirstlane_b32 s22, v189
	s_ashr_i32 s23, s22, 31
	s_add_u32 s20, s3, s30
	s_addc_u32 s21, s19, s31
	s_ashr_i32 s7, s6, 31
	s_lshl_b64 s[22:23], s[22:23], 22
	s_lshl_b64 s[28:29], s[6:7], 19
	s_add_u32 s22, s33, s22
	s_addc_u32 s23, s56, s23
	s_add_u32 s22, s22, s28
	s_addc_u32 s23, s23, s29
	s_add_u32 s28, s22, 0x40000
	s_addc_u32 s29, s23, 0
	s_lshl_b64 s[36:37], s[6:7], 8
	s_add_u32 s7, s64, s30
	s_addc_u32 s31, s65, s31
	s_add_u32 s30, s7, s36
	s_addc_u32 s31, s31, s37
	s_lshl_b32 s76, s34, 8
	s_lshl_b32 s77, s6, 8
	s_mov_b64 s[34:35], -1
	s_branch .LBB0_2361
